# speedup vs baseline: 1.0017x; 1.0017x over previous
_Z6gemm_gILi64ELi128ELi32ELi64ELi0ELi2ELi64ELi3EEv5GemmP:
	s_lshl_b32 s90, s3, 7
	s_add_u32 s90, s90, s2
	s_bfe_u32 s3, s90, 0x30003
	s_lshr_b32 s91, s90, 6
	s_lshl_b32 s91, s91, 3
	s_and_b32 s2, s90, 7
	s_or_b32 s2, s2, s91
	s_load_dword s89, s[0:1], 0x40
	s_load_dword s8, s[0:1], 0x38
	s_load_dwordx4 s[4:7], s[0:1], 0x0
	v_lshrrev_b32_e32 v14, 3, v0
	v_xor_b32_e32 v1, v14, v0
	s_lshl_b32 s12, s2, 6
	v_lshlrev_b32_e32 v1, 3, v1
	v_and_b32_e32 v6, 56, v1
	v_or_b32_e32 v1, s12, v14
	s_waitcnt lgkmcnt(0)
	v_mad_u64_u32 v[2:3], s[14:15], v1, s8, v[6:7]
	v_or_b32_e32 v1, 0x100, v0
	v_lshrrev_b32_e32 v1, 3, v1
	v_xor_b32_e32 v3, v1, v0
	v_lshlrev_b32_e32 v3, 3, v3
	v_and_b32_e32 v8, 56, v3
	v_or_b32_e32 v3, s12, v1
	s_lshl_b32 s13, s3, 7
	v_mad_u64_u32 v[4:5], s[14:15], v3, s8, v[8:9]
	v_or_b32_e32 v3, s13, v14
	v_mad_i64_i32 v[10:11], s[2:3], v3, s8, 0
	v_lshl_add_u64 v[10:11], v[10:11], 1, s[6:7]
	v_lshlrev_b32_e32 v12, 1, v6
	v_mov_b32_e32 v13, 0
	v_or_b32_e32 v3, s13, v1
	v_lshl_add_u64 v[6:7], v[10:11], 0, v[12:13]
	v_mad_i64_i32 v[10:11], s[2:3], v3, s8, 0
	v_or_b32_e32 v3, 0x200, v0
	v_lshrrev_b32_e32 v15, 3, v3
	v_xor_b32_e32 v3, v15, v0
	v_lshl_add_u64 v[10:11], v[10:11], 1, s[6:7]
	v_lshlrev_b32_e32 v12, 1, v8
	v_lshlrev_b32_e32 v3, 4, v3
	v_lshl_add_u64 v[8:9], v[10:11], 0, v[12:13]
	v_and_b32_e32 v12, 0x70, v3
	v_or_b32_e32 v3, 0x300, v0
	v_or_b32_e32 v5, s13, v15
	v_lshrrev_b32_e32 v16, 3, v3
	v_mad_i64_i32 v[10:11], s[2:3], v5, s8, 0
	v_xor_b32_e32 v3, v16, v0
	v_or_b32_e32 v5, s13, v16
	s_ashr_i32 s9, s8, 31
	v_readfirstlane_b32 s10, v0
	v_lshl_add_u64 v[10:11], v[10:11], 1, s[6:7]
	v_mad_i64_i32 v[18:19], s[2:3], v5, s8, 0
	v_lshlrev_b32_e32 v3, 4, v3
	v_cmp_gt_i64_e64 s[16:17], s[8:9], 63
	v_lshl_add_u64 v[10:11], v[10:11], 0, v[12:13]
	v_lshl_add_u64 v[18:19], v[18:19], 1, s[6:7]
	v_and_b32_e32 v12, 0x70, v3
	s_lshl_b32 s2, s10, 4
	v_lshl_add_u64 v[12:13], v[18:19], 0, v[12:13]
	s_and_b32 s15, s2, 0xfffffc00
	s_mov_b32 s6, 0
	s_and_b64 vcc, exec, s[16:17]
	s_cbranch_vccz .LBB8_2
	v_ashrrev_i32_e32 v3, 31, v2
	s_mov_b32 m0, s15
	v_lshl_add_u64 v[18:19], v[2:3], 1, s[4:5]
	v_ashrrev_i32_e32 v5, 31, v4
	global_load_lds_dwordx4 v[18:19], off
	v_lshl_add_u64 v[18:19], v[4:5], 1, s[4:5]
	s_add_i32 m0, s15, 0x1000
	s_mov_b32 s6, 64
	global_load_lds_dwordx4 v[18:19], off
	s_add_i32 m0, s15, 0x2000
	s_nop 0
	global_load_lds_dwordx4 v[6:7], off
	s_add_i32 m0, s15, 0x3000
	s_nop 0
	global_load_lds_dwordx4 v[8:9], off
	s_add_i32 m0, s15, 0x4000
	s_nop 0
	global_load_lds_dwordx4 v[10:11], off
	s_add_i32 m0, s15, 0x5000
	s_nop 0
	global_load_lds_dwordx4 v[12:13], off

.LBB8_17:
	s_mov_b32 s0, s89
	s_lshl_b32 s1, s14, 1
	v_lshlrev_b32_e32 v3, 3, v3
	v_mul_i32_i24_e32 v17, 0x90, v17
	v_accvgpr_read_b32 v11, a20
	v_accvgpr_read_b32 v12, a21
	v_accvgpr_read_b32 v13, a22
	v_accvgpr_read_b32 v18, a23
	v_accvgpr_read_b32 v31, a4
	v_accvgpr_read_b32 v32, a5
	v_accvgpr_read_b32 v33, a6
	v_accvgpr_read_b32 v34, a7
	v_add3_u32 v17, s1, v3, v17
	s_ashr_i32 s1, s12, 12
	v_accvgpr_read_b32 v7, a24
	v_accvgpr_read_b32 v8, a25
	v_accvgpr_read_b32 v9, a26
	v_accvgpr_read_b32 v10, a27
	v_accvgpr_read_b32 v27, a8
	v_accvgpr_read_b32 v28, a9
	v_accvgpr_read_b32 v29, a10
	v_accvgpr_read_b32 v30, a11
	v_cvt_pk_f16_f32 v33, v33, v34
	v_cvt_pk_f16_f32 v32, v31, v32
	v_cvt_pk_f16_f32 v13, v13, v18
	v_cvt_pk_f16_f32 v12, v11, v12
	v_add_u32_e32 v3, 0x800, v17
	s_and_b32 s5, s12, 0xfc0
	s_waitcnt lgkmcnt(0)
	s_mul_i32 s0, s0, s1
	v_accvgpr_read_b32 v5, a30
	v_accvgpr_read_b32 v6, a31
	s_waitcnt vmcnt(0)
	s_barrier
	v_cvt_pk_f16_f32 v29, v29, v30
	v_cvt_pk_f16_f32 v28, v27, v28
	ds_write2_b64 v3, v[32:33], v[12:13] offset0:32 offset1:36
	v_cvt_pk_f16_f32 v9, v9, v10
	v_cvt_pk_f16_f32 v8, v7, v8
	v_add_u32_e32 v3, 0x1000, v17
	v_lshlrev_b32_e32 v0, 4, v0
	s_add_i32 s6, s0, s13
	s_lshl_b32 s0, s5, 1
	v_accvgpr_read_b32 v2, a28
	v_accvgpr_read_b32 v4, a29
	v_accvgpr_read_b32 v19, a16
	v_accvgpr_read_b32 v20, a17
	v_accvgpr_read_b32 v21, a18
	v_accvgpr_read_b32 v22, a19
	v_accvgpr_read_b32 v23, a12
	v_accvgpr_read_b32 v24, a13
	v_accvgpr_read_b32 v25, a14
	v_accvgpr_read_b32 v26, a15
	v_accvgpr_read_b32 v35, a0
	v_accvgpr_read_b32 v36, a1
	v_accvgpr_read_b32 v37, a2
	v_accvgpr_read_b32 v38, a3
	s_movk_i32 s4, 0x90
	ds_write2_b64 v3, v[28:29], v[8:9] offset0:64 offset1:68
	v_cvt_pk_f16_f32 v3, v5, v6
	v_and_b32_e32 v10, 0x70, v0
	s_add_u32 s0, s2, s0
	v_add_u32_e32 v6, s6, v14
	v_cvt_pk_f16_f32 v37, v37, v38
	v_cvt_pk_f16_f32 v36, v35, v36
	v_cvt_pk_f16_f32 v25, v25, v26
	v_cvt_pk_f16_f32 v24, v23, v24
	v_cvt_pk_f16_f32 v21, v21, v22
	v_cvt_pk_f16_f32 v20, v19, v20
	v_cvt_pk_f16_f32 v2, v2, v4
	v_add_u32_e32 v4, 0x1800, v17
	s_addc_u32 s1, s3, 0
	v_mov_b32_e32 v11, 0
	v_mad_u32_u24 v0, v14, s4, v10
	v_ashrrev_i32_e32 v7, 31, v6
	ds_write2_b64 v17, v[36:37], v[20:21] offset1:4
	ds_write2_b64 v4, v[24:25], v[2:3] offset0:96 offset1:100
	s_waitcnt lgkmcnt(0)
	s_barrier
	v_lshl_add_u64 v[12:13], s[0:1], 0, v[10:11]
	ds_read_b128 v[2:5], v0
	v_lshlrev_b64 v[6:7], 13, v[6:7]
	v_mad_u32_u24 v0, v1, s4, v10
	v_lshl_add_u64 v[18:19], v[12:13], 0, v[6:7]
	ds_read_b128 v[6:9], v0
	v_add_u32_e32 v0, s6, v1
	v_ashrrev_i32_e32 v1, 31, v0
	v_lshlrev_b64 v[0:1], 13, v[0:1]
	v_lshl_add_u64 v[0:1], v[12:13], 0, v[0:1]
	s_waitcnt lgkmcnt(1)
	global_store_dwordx4 v[18:19], v[2:5], off
	s_waitcnt lgkmcnt(0)
	global_store_dwordx4 v[0:1], v[6:9], off
	v_mad_u32_u24 v0, v15, s4, v10
	ds_read_b128 v[0:3], v0
	v_add_u32_e32 v4, s6, v15
	v_ashrrev_i32_e32 v5, 31, v4
	v_lshlrev_b64 v[4:5], 13, v[4:5]
	v_lshl_add_u64 v[8:9], v[12:13], 0, v[4:5]
	v_mad_u32_u24 v4, v16, s4, v10
	ds_read_b128 v[4:7], v4
	s_waitcnt lgkmcnt(1)
	global_store_dwordx4 v[8:9], v[0:3], off
	s_nop 1
	v_add_u32_e32 v0, s6, v16
	v_ashrrev_i32_e32 v1, 31, v0
	v_lshlrev_b64 v[0:1], 13, v[0:1]
	v_lshl_add_u64 v[0:1], v[12:13], 0, v[0:1]
	s_waitcnt lgkmcnt(0)
	global_store_dwordx4 v[0:1], v[4:7], off
	s_endpgm

_Z6gemm_gILi64ELi64ELi32ELi32ELi0ELi4ELi64ELi3EEv5GemmP:
	s_load_dword s89, s[0:1], 0x40
	s_load_dword s10, s[0:1], 0x38
	s_load_dwordx4 s[4:7], s[0:1], 0x0
	v_lshrrev_b32_e32 v1, 3, v0
	v_xor_b32_e32 v2, v1, v0
	s_lshl_b32 s2, s2, 6
	v_lshlrev_b32_e32 v2, 3, v2
	v_and_b32_e32 v6, 56, v2
	v_or_b32_e32 v11, s2, v1
	s_waitcnt lgkmcnt(0)
	v_mad_u64_u32 v[2:3], s[16:17], v11, s10, v[6:7]
	v_or_b32_e32 v3, 0x100, v0
	v_lshrrev_b32_e32 v10, 3, v3
	v_xor_b32_e32 v3, v10, v0
	v_lshlrev_b32_e32 v3, 3, v3
	v_or_b32_e32 v12, s2, v10
	s_lshl_b32 s2, s3, 6
	v_and_b32_e32 v8, 56, v3
	v_or_b32_e32 v3, s2, v1
	v_mad_i64_i32 v[14:15], s[16:17], v3, s10, 0
	v_lshl_add_u64 v[14:15], v[14:15], 1, s[6:7]
	v_lshlrev_b32_e32 v16, 1, v6
	v_mov_b32_e32 v17, 0
	v_or_b32_e32 v3, s2, v10
	s_ashr_i32 s11, s10, 31
	v_readfirstlane_b32 s12, v0
	v_lshl_add_u64 v[6:7], v[14:15], 0, v[16:17]
	v_mad_i64_i32 v[14:15], s[16:17], v3, s10, 0
	v_cmp_gt_i64_e64 s[14:15], s[10:11], 63
	s_lshr_b32 s9, s12, 6
	v_lshl_add_u64 v[14:15], v[14:15], 1, s[6:7]
	v_lshlrev_b32_e32 v16, 1, v8
	v_mad_u64_u32 v[4:5], s[16:17], v12, s10, v[8:9]
	v_lshl_add_u64 v[8:9], v[14:15], 0, v[16:17]
	s_lshl_b32 s3, s9, 10
	s_mov_b32 s8, 0
	s_and_b64 vcc, exec, s[14:15]
	s_cbranch_vccz .LBB10_2
	v_ashrrev_i32_e32 v3, 31, v2
	s_mov_b32 m0, s3
	v_lshl_add_u64 v[14:15], v[2:3], 1, s[4:5]
	v_ashrrev_i32_e32 v5, 31, v4
	global_load_lds_dwordx4 v[14:15], off
	v_lshl_add_u64 v[14:15], v[4:5], 1, s[4:5]
	s_add_i32 m0, s3, 0x1000
	s_mov_b32 s8, 64
	global_load_lds_dwordx4 v[14:15], off
	s_add_i32 m0, s3, 0x2000
	s_nop 0
	global_load_lds_dwordx4 v[6:7], off
	s_add_i32 m0, s3, 0x3000
	s_nop 0
	global_load_lds_dwordx4 v[8:9], off

.LBB10_13:
	s_nop 3
	v_accvgpr_read_b32 v22, a0
	v_lshl_or_b32 v5, v5, 2, s12
	s_movk_i32 s4, 0x90
	s_mov_b32 s0, s89
	v_accvgpr_read_b32 v21, a1
	s_lshl_b32 s1, s13, 1
	v_lshlrev_b32_e32 v3, 1, v3
	v_cvt_f16_f32_e32 v22, v22
	v_mul_lo_u32 v5, v5, s4
	v_accvgpr_read_b32 v20, a2
	v_add3_u32 v3, s1, v3, v5
	v_cvt_f16_f32_e32 v5, v21
	v_accvgpr_read_b32 v19, a3
	v_cvt_f16_f32_e32 v20, v20
	v_accvgpr_read_b32 v18, a4
	v_cvt_f16_f32_e32 v19, v19
	v_accvgpr_read_b32 v17, a5
	s_waitcnt vmcnt(0) lgkmcnt(0)
	s_barrier
	ds_write_b16 v3, v22
	ds_write_b16 v3, v5 offset:144
	ds_write_b16 v3, v20 offset:288
	ds_write_b16 v3, v19 offset:432
	v_cvt_f16_f32_e32 v5, v18
	v_accvgpr_read_b32 v16, a6
	v_cvt_f16_f32_e32 v17, v17
	v_accvgpr_read_b32 v15, a7
	v_cvt_f16_f32_e32 v16, v16
	v_accvgpr_read_b32 v14, a8
	v_cvt_f16_f32_e32 v15, v15
	v_accvgpr_read_b32 v13, a9
	ds_write_b16 v3, v5 offset:32
	ds_write_b16 v3, v17 offset:176
	ds_write_b16 v3, v16 offset:320
	ds_write_b16 v3, v15 offset:464
	v_cvt_f16_f32_e32 v5, v14
	v_accvgpr_read_b32 v9, a10
	v_cvt_f16_f32_e32 v13, v13
	v_accvgpr_read_b32 v8, a11
	v_cvt_f16_f32_e32 v9, v9
	v_accvgpr_read_b32 v7, a12
	v_cvt_f16_f32_e32 v8, v8
	v_accvgpr_read_b32 v6, a13
	ds_write_b16 v3, v5 offset:2304
	ds_write_b16 v3, v13 offset:2448
	ds_write_b16 v3, v9 offset:2592
	ds_write_b16 v3, v8 offset:2736
	v_cvt_f16_f32_e32 v5, v7
	v_accvgpr_read_b32 v4, a14
	v_cvt_f16_f32_e32 v6, v6
	v_accvgpr_read_b32 v2, a15
	v_cvt_f16_f32_e32 v4, v4
	v_cvt_f16_f32_e32 v2, v2
	v_lshlrev_b32_e32 v0, 4, v0
	s_ashr_i32 s3, s2, 31
	ds_write_b16 v3, v5 offset:2336
	ds_write_b16 v3, v6 offset:2480
	ds_write_b16 v3, v4 offset:2624
	ds_write_b16 v3, v2 offset:2768
	v_and_b32_e32 v4, 0x70, v0
	s_lshl_b64 s[2:3], s[2:3], 1
	s_add_u32 s2, s6, s2
	v_mad_u32_u24 v0, v1, s4, v4
	s_waitcnt lgkmcnt(0)
	s_barrier
	s_addc_u32 s3, s7, s3
	v_mov_b32_e32 v5, 0
	ds_read_b128 v[0:3], v0
	v_lshl_add_u64 v[8:9], s[2:3], 0, v[4:5]
	v_mad_i64_i32 v[6:7], s[2:3], v11, s0, 0
	v_mad_u32_u24 v4, v10, s4, v4
	v_lshl_add_u64 v[14:15], v[6:7], 1, v[8:9]
	ds_read_b128 v[4:7], v4
	s_waitcnt lgkmcnt(1)
	global_store_dwordx4 v[14:15], v[0:3], off
	s_nop 1
	v_mad_i64_i32 v[0:1], s[0:1], v12, s0, 0
	v_lshl_add_u64 v[0:1], v[0:1], 1, v[8:9]
	s_waitcnt lgkmcnt(0)
	global_store_dwordx4 v[0:1], v[4:7], off
	s_endpgm
